# MLA fast88 loop: K-fragment ds_reads of the next tile hoisted to the top of each half-iteration (before the K/V DMA issue blocks)
# speedup vs baseline: 1.0116x; 1.0116x over previous
; #define ALAS __attribute__((address_space(3)))
; #define MF_ISSUE_K(t, s) do { glds16(ksrc + (long)(t) * 64 * 512, (unsigned)__builtin_amdgcn_readfirstlane(kdst + (s) * KSLOT)); \
;         if (wid < 4) glds16(krsrc + (long)(t) * 64 * 32, (unsigned)__builtin_amdgcn_readfirstlane(krdst + (s) * KSLOT)); } while (0)
; #define MF_ISSUE_V(t, s) glds16(vsrc + (long)(t) * 64 * 512, (unsigned)__builtin_amdgcn_readfirstlane(vdst + (s) * VSLOT))
; #define MF_ISSUE_K(t, s) glds16(ks8 + (long)(t) * kst8, (unsigned)__builtin_amdgcn_readfirstlane(kdst + (s) * KSLOT))
; #define MF_ISSUE_V(t, s) glds16(vsrc + (long)(t) * 64 * 512, (unsigned)__builtin_amdgcn_readfirstlane(vdst + (s) * VSLOT))
; #define M8_KFRAG(dst, base, m, kh) do { const u32x4 lo_ = *(ALAS const u32x4*)((base) + (((m) * 2 + (kh)) * 2) * 1024), hi_ = *(ALAS const u32x4*)((base) + (((m) * 2 + (kh)) * 2 + 1) * 1024); \
;         dst = (v8i){(int)lo_.x, (int)lo_.y, (int)lo_.z, (int)lo_.w, (int)hi_.x, (int)hi_.y, (int)hi_.z, (int)hi_.w}; } while (0)
; #define MF_ISSUE_K(t, s) glds16(ks8 + (long)(t) * kst8, (unsigned)__builtin_amdgcn_readfirstlane(kdst + (s) * KSLOT))
; #define MF_ISSUE_V(t, s) do { if (wid < 4) glds16(vs8 + (long)(t) * 4096, (unsigned)__builtin_amdgcn_readfirstlane(vdst + (s) * 4096)); } while (0)
; #define M8_KFRAG(dst, base, m, kh) do { const u32x4 lo_ = *(ALAS const u32x4*)((base) + (((m) * 2 + (kh)) * 2) * 1024), hi_ = *(ALAS const u32x4*)((base) + (((m) * 2 + (kh)) * 2 + 1) * 1024); \
;         dst = (v8i){(int)lo_.x, (int)lo_.y, (int)lo_.z, (int)lo_.w, (int)hi_.x, (int)hi_.y, (int)hi_.z, (int)hi_.w}; } while (0)
; __device__ __forceinline__ bool mla_unit_fast88(const Args& A, int b, int h, int qb, ALAS char* shm, const int tidb) {
;     ...
;         for (int p = 0; p < 2; ++p) {
;             const int t = t2 + p; f32x16 &C0 = cs[p][0], &C1 = cs[p][1], &N0 = cs[p ^ 1][0], &N1 = cs[p ^ 1][1];
;             const bool vis = !bailed && t <= cw;
;             const int ks1 = ks == 2 ? 0 : ks + 1, ks2 = ks1 == 2 ? 0 : ks1 + 1;
;             if (t + 2 < t_end) MF_ISSUE_K(t + 2, ks2);
;             if (t + 1 < t_end) MF_ISSUE_V(t + 1, vs ^ 1);
;             if (vis) {
;                 {
;                     ALAS const char* Ks_ = Kfr + ks1 * KSLOT;
;                     v8i kfa, kfb; M8_KFRAG(kfa, Ks_, 0, 0);
;                     M8_KFRAG(kfb, Ks_, 0, 1);
.LBB0_649:
	s_add_i32 s2, s4, 1
	s_cmp_lg_u32 s4, 2
	s_cselect_b32 s4, s2, 0
	v_lshl_add_u32 v171, s4, 13, v157
	ds_read_b128 v[114:117], v171
	ds_read_b128 v[118:121], v171 offset:1024
	ds_read_b128 v[164:167], v171 offset:2048
	ds_read_b128 v[168:171], v171 offset:3072
	s_add_i32 s6, s5, -1
	s_cmp_lt_u32 s6, s0
	s_cselect_b64 s[2:3], -1, 0
	s_and_b64 vcc, exec, s[2:3]
	v_lshl_add_u64 v[152:153], v[146:147], 0, v[0:1]
	s_cbranch_vccz .LBB0_651
	s_lshl_b32 s7, s4, 13
	s_addk_i32 s7, 0x2000
	s_cmp_lg_u32 s4, 2
	s_cselect_b32 s7, s7, 0
	v_lshl_add_u64 v[158:159], v[146:147], 0, v[0:1]
	s_add_i32 s7, s7, s45
	s_mov_b32 s8, m0
	s_mov_b32 m0, s7
	s_nop 0
	global_load_lds_dwordx4 v[158:159], off
	s_mov_b32 m0, s8

; #define ALAS __attribute__((address_space(3)))
; __device__ __forceinline__ bool mla_unit_fast88(const Args& A, int b, int h, int qb, ALAS char* shm, const int tidb) {
;     ...
;             if (vis) {
;                 {
;                     ALAS const char* Ks_ = Kfr + ks1 * KSLOT;
;                     v8i kfa, kfb; M8_KFRAG(kfa, Ks_, 0, 0);
;                     M8_KFRAG(kfb, Ks_, 0, 1);
;                     mfma8_new(N0, kfa, qf0, negm, sa8, sb8);
; #pragma unroll
;                     for (int e = 0; e < 8; ++e) C0[e] = __builtin_amdgcn_exp2f(C0[e]);
;                     __builtin_amdgcn_sched_barrier(0);
;                     M8_KFRAG(kfa, Ks_, 1, 0);
;                     mfma8_new(N1, kfb, qf0, negm, sa8, sb8);
; #pragma unroll
;                     for (int e = 8; e < 16; ++e) C0[e] = __builtin_amdgcn_exp2f(C0[e]);
;                     __builtin_amdgcn_sched_barrier(0);
;                     M8_KFRAG(kfb, Ks_, 1, 1);
;                     mfma8_acc(N0, kfa, qf1, sa8, sb8);
; #pragma unroll
;                     for (int e = 0; e < 8; ++e) C1[e] = __builtin_amdgcn_exp2f(C1[e]);
;                     __builtin_amdgcn_sched_barrier(0);
;                     mfma8_acc(N1, kfb, qf1, sa8, sb8);
; #pragma unroll
;                     for (int e = 8; e < 16; ++e) C1[e] = __builtin_amdgcn_exp2f(C1[e]);
;                     __builtin_amdgcn_sched_barrier(0);
;                 }
;                 ALAS const char* vb_ = shm + L_V + vs * 4096 + lane * 16;
;                 v8i vf0, vf1;
;                 { const u32x4 a0 = *(ALAS const u32x4*)(vb_), a1 = *(ALAS const u32x4*)(vb_ + 1024), b0 = *(ALAS const u32x4*)(vb_ + 2048), b1 = *(ALAS const u32x4*)(vb_ + 3072);
;                   vf0 = (v8i){(int)a0.x, (int)a0.y, (int)a0.z, (int)a0.w, (int)a1.x, (int)a1.y, (int)a1.z, (int)a1.w}; vf1 = (v8i){(int)b0.x, (int)b0.y, (int)b0.z, (int)b0.w, (int)b1.x, (int)b1.y, (int)b1.z, (int)b1.w}; }
;                 v8i pf;
; #pragma unroll
;                 for (int kk = 0; kk < 4; ++kk) { const f32x16& cc_ = (kk < 2) ? C0 : C1; const int k8_ = 8 * (kk & 1);
;                     int w0_ = 0, w1_ = 0;
;                     w0_ = __builtin_amdgcn_cvt_pk_bf8_f32(cc_[k8_], cc_[k8_ + 1], w0_, false); w0_ = __builtin_amdgcn_cvt_pk_bf8_f32(cc_[k8_ + 2], cc_[k8_ + 3], w0_, true);
.LBB0_653:
	s_add_i32 s7, s5, -3
	s_cmp_gt_i32 s7, s47
	s_cbranch_scc1 .LBB0_655
	v_lshl_add_u32 v158, s4, 13, v157
	v_exp_f32_e32 v50, v50
	v_exp_f32_e32 v51, v51
	v_exp_f32_e32 v52, v52
	v_exp_f32_e32 v53, v53
	v_exp_f32_e32 v54, v54
	v_exp_f32_e32 v55, v55
	v_exp_f32_e32 v56, v56
	v_exp_f32_e32 v57, v57
	s_waitcnt lgkmcnt(2)
	v_mfma_scale_f32_32x32x64_f8f6f4 v[98:113], v[114:121], v[130:137], v[66:81], v247, v253 op_sel_hi:[0,0,0]
	ds_read_b128 v[172:175], v158 offset:4096
	ds_read_b128 v[176:179], v158 offset:5120
	v_exp_f32_e32 v58, v58
	v_exp_f32_e32 v59, v59
	v_exp_f32_e32 v60, v60
	v_exp_f32_e32 v61, v61
	v_exp_f32_e32 v62, v62
	v_exp_f32_e32 v63, v63
	v_exp_f32_e32 v64, v64
	v_exp_f32_e32 v65, v65
	s_waitcnt lgkmcnt(2)
	v_mfma_scale_f32_32x32x64_f8f6f4 v[114:129], v[164:171], v[130:137], v[66:81], v247, v253 op_sel_hi:[0,0,0]
	ds_read_b128 v[164:167], v158 offset:6144
	ds_read_b128 v[168:171], v158 offset:7168
	v_exp_f32_e32 v82, v82
	v_exp_f32_e32 v83, v83
	v_exp_f32_e32 v84, v84
	v_exp_f32_e32 v85, v85
	v_exp_f32_e32 v86, v86
	v_exp_f32_e32 v87, v87
	v_exp_f32_e32 v88, v88
	v_exp_f32_e32 v89, v89
	s_waitcnt lgkmcnt(2)
	v_mfma_scale_f32_32x32x64_f8f6f4 v[98:113], v[172:179], v[138:145], v[98:113], v247, v253 op_sel_hi:[0,0,0]
	v_exp_f32_e32 v90, v90
	v_exp_f32_e32 v91, v91
	v_exp_f32_e32 v92, v92
	v_exp_f32_e32 v93, v93
	v_exp_f32_e32 v94, v94
	v_exp_f32_e32 v95, v95
	v_exp_f32_e32 v96, v96
	v_exp_f32_e32 v97, v97
	s_waitcnt lgkmcnt(0)
	v_mfma_scale_f32_32x32x64_f8f6f4 v[114:129], v[164:171], v[138:145], v[114:129], v247, v253 op_sel_hi:[0,0,0]
	ds_read_b128 v[164:167], v157 offset:36864
	ds_read_b128 v[168:171], v157 offset:37888
	ds_read_b128 v[172:175], v157 offset:38912
	ds_read_b128 v[176:179], v157 offset:39936
	v_mov_b32_e32 v180, 0
	v_mov_b32_e32 v181, 0
	v_mov_b32_e32 v182, 0
	v_mov_b32_e32 v183, 0
	v_mov_b32_e32 v184, 0
	v_mov_b32_e32 v185, 0
	v_mov_b32_e32 v186, 0
	v_mov_b32_e32 v187, 0
	v_cvt_pk_bf8_f32 v180, v50, v51
	v_cvt_pk_bf8_f32 v181, v54, v55
	v_cvt_pk_bf8_f32 v182, v58, v59
	v_cvt_pk_bf8_f32 v183, v62, v63
	v_cvt_pk_bf8_f32 v184, v82, v83
	v_cvt_pk_bf8_f32 v185, v86, v87
	v_cvt_pk_bf8_f32 v186, v90, v91
	v_cvt_pk_bf8_f32 v187, v94, v95
	v_cvt_pk_bf8_f32 v180, v52, v53 op_sel:[0,0,1]
	v_cvt_pk_bf8_f32 v181, v56, v57 op_sel:[0,0,1]
	v_cvt_pk_bf8_f32 v182, v60, v61 op_sel:[0,0,1]
	v_cvt_pk_bf8_f32 v183, v64, v65 op_sel:[0,0,1]
	v_cvt_pk_bf8_f32 v184, v84, v85 op_sel:[0,0,1]
	v_cvt_pk_bf8_f32 v185, v88, v89 op_sel:[0,0,1]
	v_cvt_pk_bf8_f32 v186, v92, v93 op_sel:[0,0,1]
	v_cvt_pk_bf8_f32 v187, v96, v97 op_sel:[0,0,1]
	s_waitcnt lgkmcnt(2)
	v_mfma_scale_f32_32x32x64_f8f6f4 v[2:17], v[180:187], v[164:171], v[2:17], v251, v247 op_sel_hi:[0,0,0] cbsz:1
	s_waitcnt lgkmcnt(0)
	v_mfma_scale_f32_32x32x64_f8f6f4 v[18:33], v[180:187], v[172:179], v[18:33], v251, v247 op_sel_hi:[0,0,0] cbsz:1
	v_mov_b32_e32 v163, v162
	v_mov_b32_e32 v164, v162
	v_mov_b32_e32 v165, v162
	v_mov_b32_e32 v166, v162
	v_mov_b32_e32 v167, v162
	v_mov_b32_e32 v168, v162
	v_mov_b32_e32 v169, v162
	v_mfma_scale_f32_32x32x64_f8f6f4 v[34:49], v[180:187], v[162:169], v[34:49], v251, v251 op_sel_hi:[0,0,0] cbsz:1
.LBB0_655:
	s_add_i32 s8, s4, 1
	s_waitcnt vmcnt(0) lgkmcnt(0)
	s_barrier
	s_cmp_lg_u32 s4, 2
	s_cselect_b32 s4, s8, 0
	v_lshl_add_u32 v171, s4, 13, v157
	ds_read_b128 v[82:85], v171
	ds_read_b128 v[86:89], v171 offset:1024
	ds_read_b128 v[164:167], v171 offset:2048
	ds_read_b128 v[168:171], v171 offset:3072
	s_cmp_ge_u32 s5, s0
	s_cbranch_scc1 .LBB0_661
	s_lshl_b32 s8, s4, 13
	s_addk_i32 s8, 0x2000
	s_cmp_lg_u32 s4, 2
	s_cselect_b32 s8, s8, 0
	v_lshl_add_u64 v[146:147], v[146:147], 0, v[148:149]
	s_add_i32 s8, s8, s45
	s_mov_b32 s9, m0
	s_mov_b32 m0, s8
	s_nop 0
	global_load_lds_dwordx4 v[146:147], off
	s_mov_b32 m0, s9
	s_and_b64 s[2:3], s[34:35], s[2:3]
	s_andn2_b64 vcc, exec, s[2:3]
	s_cbranch_vccz .LBB0_662

; #define ALAS __attribute__((address_space(3)))
; __device__ __forceinline__ bool mla_unit_fast88(const Args& A, int b, int h, int qb, ALAS char* shm, const int tidb) {
;     ...
;             if (vis) {
;                 {
;                     ALAS const char* Ks_ = Kfr + ks1 * KSLOT;
;                     v8i kfa, kfb; M8_KFRAG(kfa, Ks_, 0, 0);
;                     M8_KFRAG(kfb, Ks_, 0, 1);
;                     mfma8_new(N0, kfa, qf0, negm, sa8, sb8);
; #pragma unroll
;                     for (int e = 0; e < 8; ++e) C0[e] = __builtin_amdgcn_exp2f(C0[e]);
;                     __builtin_amdgcn_sched_barrier(0);
;                     M8_KFRAG(kfa, Ks_, 1, 0);
;                     mfma8_new(N1, kfb, qf0, negm, sa8, sb8);
; #pragma unroll
;                     for (int e = 8; e < 16; ++e) C0[e] = __builtin_amdgcn_exp2f(C0[e]);
;                     __builtin_amdgcn_sched_barrier(0);
;                     M8_KFRAG(kfb, Ks_, 1, 1);
;                     mfma8_acc(N0, kfa, qf1, sa8, sb8);
; #pragma unroll
;                     for (int e = 0; e < 8; ++e) C1[e] = __builtin_amdgcn_exp2f(C1[e]);
;                     __builtin_amdgcn_sched_barrier(0);
;                     mfma8_acc(N1, kfb, qf1, sa8, sb8);
; #pragma unroll
;                     for (int e = 8; e < 16; ++e) C1[e] = __builtin_amdgcn_exp2f(C1[e]);
;                     __builtin_amdgcn_sched_barrier(0);
;                 }
;                 ALAS const char* vb_ = shm + L_V + vs * 4096 + lane * 16;
;                 v8i vf0, vf1;
;                 { const u32x4 a0 = *(ALAS const u32x4*)(vb_), a1 = *(ALAS const u32x4*)(vb_ + 1024), b0 = *(ALAS const u32x4*)(vb_ + 2048), b1 = *(ALAS const u32x4*)(vb_ + 3072);
;                   vf0 = (v8i){(int)a0.x, (int)a0.y, (int)a0.z, (int)a0.w, (int)a1.x, (int)a1.y, (int)a1.z, (int)a1.w}; vf1 = (v8i){(int)b0.x, (int)b0.y, (int)b0.z, (int)b0.w, (int)b1.x, (int)b1.y, (int)b1.z, (int)b1.w}; }
;                 v8i pf;
; #pragma unroll
;                 for (int kk = 0; kk < 4; ++kk) { const f32x16& cc_ = (kk < 2) ? C0 : C1; const int k8_ = 8 * (kk & 1);
;                     int w0_ = 0, w1_ = 0;
;                     w0_ = __builtin_amdgcn_cvt_pk_bf8_f32(cc_[k8_], cc_[k8_ + 1], w0_, false); w0_ = __builtin_amdgcn_cvt_pk_bf8_f32(cc_[k8_ + 2], cc_[k8_ + 3], w0_, true);
.LBB0_658:
	v_lshl_add_u32 v146, s4, 13, v157
	v_exp_f32_e32 v98, v98
	v_exp_f32_e32 v99, v99
	v_exp_f32_e32 v100, v100
	v_exp_f32_e32 v101, v101
	v_exp_f32_e32 v102, v102
	v_exp_f32_e32 v103, v103
	v_exp_f32_e32 v104, v104
	v_exp_f32_e32 v105, v105
	s_waitcnt lgkmcnt(2)
	v_mfma_scale_f32_32x32x64_f8f6f4 v[50:65], v[82:89], v[130:137], v[66:81], v247, v253 op_sel_hi:[0,0,0]
	ds_read_b128 v[172:175], v146 offset:4096
	ds_read_b128 v[176:179], v146 offset:5120
	v_exp_f32_e32 v106, v106
	v_exp_f32_e32 v107, v107
	v_exp_f32_e32 v108, v108
	v_exp_f32_e32 v109, v109
	v_exp_f32_e32 v110, v110
	v_exp_f32_e32 v111, v111
	v_exp_f32_e32 v112, v112
	v_exp_f32_e32 v113, v113
	s_waitcnt lgkmcnt(2)
	v_mfma_scale_f32_32x32x64_f8f6f4 v[82:97], v[164:171], v[130:137], v[66:81], v247, v253 op_sel_hi:[0,0,0]
	ds_read_b128 v[164:167], v146 offset:6144
	ds_read_b128 v[168:171], v146 offset:7168
	v_exp_f32_e32 v114, v114
	v_exp_f32_e32 v115, v115
	v_exp_f32_e32 v116, v116
	v_exp_f32_e32 v117, v117
	v_exp_f32_e32 v118, v118
	v_exp_f32_e32 v119, v119
	v_exp_f32_e32 v120, v120
	v_exp_f32_e32 v121, v121
	s_waitcnt lgkmcnt(2)
	v_mfma_scale_f32_32x32x64_f8f6f4 v[50:65], v[172:179], v[138:145], v[50:65], v247, v253 op_sel_hi:[0,0,0]
	v_exp_f32_e32 v122, v122
	v_exp_f32_e32 v123, v123
	v_exp_f32_e32 v124, v124
	v_exp_f32_e32 v125, v125
	v_exp_f32_e32 v126, v126
	v_exp_f32_e32 v127, v127
	v_exp_f32_e32 v128, v128
	v_exp_f32_e32 v129, v129
	s_waitcnt lgkmcnt(0)
	v_mfma_scale_f32_32x32x64_f8f6f4 v[82:97], v[164:171], v[138:145], v[82:97], v247, v253 op_sel_hi:[0,0,0]
	ds_read_b128 v[164:167], v157 offset:40960
	ds_read_b128 v[168:171], v157 offset:41984
	ds_read_b128 v[172:175], v157 offset:43008
	ds_read_b128 v[176:179], v157 offset:44032
	v_mov_b32_e32 v180, 0
	v_mov_b32_e32 v181, 0
	v_mov_b32_e32 v182, 0
	v_mov_b32_e32 v183, 0
	v_mov_b32_e32 v184, 0
	v_mov_b32_e32 v185, 0
	v_mov_b32_e32 v186, 0
	v_mov_b32_e32 v187, 0
	v_cvt_pk_bf8_f32 v180, v98, v99
	v_cvt_pk_bf8_f32 v181, v102, v103
	v_cvt_pk_bf8_f32 v182, v106, v107
	v_cvt_pk_bf8_f32 v183, v110, v111
	v_cvt_pk_bf8_f32 v184, v114, v115
	v_cvt_pk_bf8_f32 v185, v118, v119
	v_cvt_pk_bf8_f32 v186, v122, v123
	v_cvt_pk_bf8_f32 v187, v126, v127
	v_cvt_pk_bf8_f32 v180, v100, v101 op_sel:[0,0,1]
	v_cvt_pk_bf8_f32 v181, v104, v105 op_sel:[0,0,1]
	v_cvt_pk_bf8_f32 v182, v108, v109 op_sel:[0,0,1]
	v_cvt_pk_bf8_f32 v183, v112, v113 op_sel:[0,0,1]
	v_cvt_pk_bf8_f32 v184, v116, v117 op_sel:[0,0,1]
	v_cvt_pk_bf8_f32 v185, v120, v121 op_sel:[0,0,1]
	v_cvt_pk_bf8_f32 v186, v124, v125 op_sel:[0,0,1]
	v_cvt_pk_bf8_f32 v187, v128, v129 op_sel:[0,0,1]
	s_waitcnt lgkmcnt(2)
	v_mfma_scale_f32_32x32x64_f8f6f4 v[2:17], v[180:187], v[164:171], v[2:17], v251, v247 op_sel_hi:[0,0,0] cbsz:1
	s_waitcnt lgkmcnt(0)
	v_mfma_scale_f32_32x32x64_f8f6f4 v[18:33], v[180:187], v[172:179], v[18:33], v251, v247 op_sel_hi:[0,0,0] cbsz:1
	v_mov_b32_e32 v163, v162
	v_mov_b32_e32 v164, v162
	v_mov_b32_e32 v165, v162
	v_mov_b32_e32 v166, v162
	v_mov_b32_e32 v167, v162
	v_mov_b32_e32 v168, v162
	v_mov_b32_e32 v169, v162
	v_mfma_scale_f32_32x32x64_f8f6f4 v[34:49], v[180:187], v[162:169], v[34:49], v251, v251 op_sel_hi:[0,0,0] cbsz:1
